# baseline (speedup 1.0000x reference)
.LBB1_39:
	s_or_b64 exec, exec, s[6:7]
	s_movk_i32 s3, 0xbf
	v_cmp_lt_u32_e64 s[6:7], s3, v0
	s_movk_i32 s3, 0xc0
	v_cmp_gt_u32_e32 vcc, s3, v0
	s_and_saveexec_b64 s[8:9], vcc
	s_setprio 3
	s_or_b64 exec, exec, s[8:9]
	v_mul_u32_u24_e32 v126, 0x90, v189
	s_add_i32 s16, 0, 0x24400
	v_lshlrev_b32_e32 v191, 2, v122
	v_lshl_add_u32 v126, v126, 1, 0
	v_lshlrev_b32_e32 v192, 3, v122
	v_lshlrev_b32_e32 v122, 4, v122
	v_lshl_or_b32 v127, v124, 4, v189
	v_lshl_add_u32 v196, v1, 4, s16
	s_movk_i32 s12, 0xff70
	v_lshlrev_b32_e32 v190, 4, v128
	v_add_u32_e32 v193, v126, v122
	v_mul_i32_i24_e32 v127, 0xd0, v127
	v_lshl_add_u32 v197, v124, 10, v196
	v_mad_i32_i24 v124, v189, s12, v126
	v_lshlrev_b32_e32 v126, 6, v128
	v_add3_u32 v194, 0, v127, v122
	v_mul_u32_u24_e32 v127, 0xe0, v189
	s_add_i32 s24, 0, 0x20c00
	v_add3_u32 v198, 0, v126, v122
	v_or_b32_e32 v126, v190, v189
	v_add3_u32 v195, s24, v127, v122
	v_mul_u32_u24_e32 v127, 0x110, v126
	v_add3_u32 v199, 0, v127, v122
	v_lshlrev_b32_e32 v127, 5, v128
	v_add3_u32 v200, v124, v127, v192
	v_lshl_add_u32 v132, v189, 6, v124
	v_add_u32_e32 v202, v124, v122
	v_or_b32_e32 v124, v191, v190
	s_movk_i32 s20, 0x50
	v_lshl_add_u32 v203, v0, 4, s16
	v_cmp_gt_u32_e64 s[16:17], 40, v124
	v_mad_u32_u24 v124, v189, s20, v132
	v_add3_u32 v205, v124, v127, v192
	v_add_u32_e32 v206, v124, v122
	v_and_b32_e32 v124, 0xc0, v0
	s_add_i32 s54, 0, 0x15400
	v_lshl_add_u32 v207, v124, 4, v196
	v_add_u16_e32 v124, -3, v128
	s_movk_i32 s22, 0xab
	v_add3_u32 v204, s54, v127, v192
	v_mul_lo_u16_sdwa v127, v124, s22 dst_sel:DWORD dst_unused:UNUSED_PAD src0_sel:BYTE_0 src1_sel:DWORD
	v_lshrrev_b16_e32 v127, 9, v127
	v_add_u32_e32 v201, v132, v122
	v_mul_lo_u16_e32 v132, 3, v127
	v_sub_u16_e32 v124, v124, v132
	v_and_b32_e32 v124, 0xff, v124
	v_lshl_or_b32 v132, v124, 4, v189
	v_mul_u32_u24_e32 v132, 0xd0, v132
	v_add3_u32 v208, 0, v132, v122
	v_lshl_or_b32 v132, v127, 4, v189
	v_mul_u32_u24_e32 v132, 0xe0, v132
	v_lshlrev_b32_e32 v117, 1, v117
	v_lshlrev_b32_e32 v121, 1, v121
	v_add3_u32 v209, s24, v132, v122
	v_mad_u32_u24 v124, v127, 3, v124
	v_add_u32_e32 v213, s24, v117
	v_add_u32_e32 v214, s24, v121
	s_add_i32 s24, 0, 0x1c400
	v_lshl_add_u32 v210, v124, 10, v196
	v_add_u32_e32 v124, 2, v128
	v_lshl_add_u32 v221, v115, 1, s24
	v_lshl_add_u32 v222, v116, 1, s24
	v_lshl_add_u32 v225, v114, 2, 0
	v_add_u32_e32 v227, s24, v122
	v_add3_u32 v114, v123, v131, v0
	s_mul_i32 s24, s2, 0x6900
	v_mul_u32_u24_e32 v115, 0x690, v130
	v_mul_lo_u16_e32 v127, 0x56, v124
	v_mov_b32_e32 v132, 3
	v_add3_u32 v114, v114, s24, v115
	v_min_u32_e32 v115, 0xc0, v0
	v_mul_lo_u16_sdwa v127, v127, v132 dst_sel:DWORD dst_unused:UNUSED_PAD src0_sel:BYTE_1 src1_sel:DWORD
	v_sub_u32_e32 v114, v114, v115
	v_sub_u16_e32 v127, v124, v127
	v_add_u32_e32 v154, 0x8c, v114
	v_add_u32_e32 v114, v125, v0
	v_mul_u32_u24_e32 v116, 0x690, v129
	v_lshlrev_b16_e32 v127, 4, v127
	s_movk_i32 s25, 0xf0
	v_add3_u32 v114, v114, s24, v116
	v_and_or_b32 v127, v127, s25, v189
	v_add_u32_e32 v224, s54, v121
	v_ashrrev_i32_e32 v121, 31, v120
	v_sub_u32_e32 v114, v114, v115
	s_mul_i32 s25, s2, 0x18000
	v_add_u32_e32 v156, 0x8c, v114
	v_lshl_add_u64 v[158:159], v[120:121], 2, s[40:41]
	v_lshl_add_u64 v[160:161], v[118:119], 2, s[40:41]
	s_movk_i32 s40, 0x1800
	v_mov_b32_e32 v114, s25
	v_mad_u32_u24 v114, v189, s40, v114
	v_or_b32_e32 v229, v114, v190
	v_mul_u32_u24_e32 v114, 0x690, v189
	v_add3_u32 v230, s24, v114, v190
	v_lshl_add_u32 v114, v128, 3, 0
	s_movk_i32 s10, 0x180
	v_cmp_eq_u32_e32 vcc, 2, v128
	v_cmp_gt_u32_e64 s[12:13], 16, v1
	v_lshlrev_b32_e32 v126, 7, v126
	s_movk_i32 s20, 0x300
	s_movk_i32 s22, 0x1c0
	v_mul_u32_u24_e32 v127, 0xd0, v127
	v_add_u32_e32 v231, 0x27400, v114
	v_mov_b32_e32 v114, 0
	s_movk_i32 s3, 0x90
	s_mov_b32 s33, 0
	v_cmp_ne_u32_e64 s[8:9], 3, v128
	v_cmp_gt_u32_e64 s[10:11], s10, v0
	s_movk_i32 s52, 0xd0
	s_movk_i32 s53, 0xe0
	s_and_b64 s[14:15], vcc, s[12:13]
	v_cmp_eq_u32_e64 s[18:19], 0, v1
	v_cmp_gt_u32_e64 s[20:21], s20, v0
	v_cmp_gt_u32_e64 s[22:23], s22, v0
	v_add3_u32 v211, 0, v127, v122
	v_lshl_add_u32 v212, v124, 10, v196
	v_add_u32_e32 v215, 0xe00, v213
	v_add_u32_e32 v216, 0x1c00, v213
	v_add_u32_e32 v217, 0x2a00, v213
	v_add_u32_e32 v218, 0xe00, v214
	v_add_u32_e32 v219, 0x1c00, v214
	v_add_u32_e32 v220, 0x2a00, v214
	v_add_u32_e32 v223, s54, v117
	v_add_u32_e32 v226, s54, v122
	v_sub_u32_e32 v228, v199, v126
	s_mov_b64 s[40:41], 0
	s_mov_b32 s55, 0xf149f2ca
	s_mov_b32 s56, 1.0
	s_movk_i32 s57, 0x46
	s_movk_i32 s58, 0x69
	v_mov_b32_e32 v232, 0x42200000
	s_mov_b32 s59, 0
	v_mov_b32_e32 v162, 0
	v_mov_b32_e32 v163, v114
	v_mov_b32_e32 v164, v114
	v_mov_b32_e32 v165, v114
	v_mov_b32_e32 v168, 0
	v_mov_b32_e32 v169, v114
	v_mov_b32_e32 v170, 0
	v_mov_b32_e32 v171, v114
	s_mov_b32 s75, 0
	s_mov_b32 s78, 0xc038aa3b
	s_mov_b32 s79, 0xc038aa3b
	s_branch .LBB1_43

.Lred_skip_0:
	s_nop 5
	v_med3_f32 v120, v120, s55, v232
	v_med3_f32 v121, v121, s55, v232
	v_mfma_f32_16x16x32_bf16 v[130:133], v[102:105], v[134:137], v[130:133]
	v_exp_f32_e32 v126, v126
	v_exp_f32_e32 v127, v127
	v_mfma_f32_16x16x32_bf16 v[130:133], v[106:109], v[138:141], v[130:133]
	v_exp_f32_e32 v116, v116
	v_exp_f32_e32 v117, v117
	v_exp_f32_e32 v120, v120
	v_exp_f32_e32 v121, v121
	v_med3_f32 v122, v122, s55, v232
	v_med3_f32 v123, v123, s55, v232
	v_pk_add_f32 v[126:127], v[126:127], 1.0 op_sel_hi:[1,0]
	v_pk_add_f32 v[134:135], v[120:121], 1.0 op_sel_hi:[1,0]
	v_pk_add_f32 v[116:117], v[116:117], 1.0 op_sel_hi:[1,0]
	v_pk_add_f32 v[120:121], v[120:121], 1.0 op_sel_hi:[1,0] neg_lo:[1,0] neg_hi:[1,0]
	v_exp_f32_e32 v128, v128
	v_exp_f32_e32 v129, v129
	v_exp_f32_e32 v118, v118
	v_exp_f32_e32 v119, v119
	v_exp_f32_e32 v122, v122
	v_exp_f32_e32 v123, v123
	v_pk_mul_f32 v[126:127], v[126:127], v[134:135]
	v_exp_f32_e32 v130, v130
	v_exp_f32_e32 v131, v131
	v_pk_add_f32 v[128:129], v[128:129], 1.0 op_sel_hi:[1,0]
	v_pk_add_f32 v[136:137], v[122:123], 1.0 op_sel_hi:[1,0]
	v_pk_add_f32 v[118:119], v[118:119], 1.0 op_sel_hi:[1,0]
	v_pk_add_f32 v[122:123], v[122:123], 1.0 op_sel_hi:[1,0] neg_lo:[1,0] neg_hi:[1,0]
	v_rcp_f32_e32 v126, v126
	v_rcp_f32_e32 v127, v127
	v_rcp_f32_e32 v116, v116
	v_rcp_f32_e32 v117, v117
	v_pk_mul_f32 v[128:129], v[128:129], v[136:137]
	v_exp_f32_e32 v132, v132
	v_exp_f32_e32 v133, v133
	v_pk_mul_f32 v[120:121], v[120:121], v[126:127]
	v_pk_add_f32 v[130:131], v[130:131], 1.0 op_sel_hi:[1,0]
	v_rcp_f32_e32 v128, v128
	v_rcp_f32_e32 v129, v129
	v_rcp_f32_e32 v118, v118
	v_rcp_f32_e32 v119, v119
	v_pk_fma_f32 v[168:169], v[168:169], v[116:117], v[120:121]
	v_pk_mul_f32 v[122:123], v[122:123], v[128:129]
	v_pk_add_f32 v[132:133], v[132:133], 1.0 op_sel_hi:[1,0]
	v_pk_mul_f32 v[134:135], v[168:169], s[78:79]
	v_pk_fma_f32 v[170:171], v[170:171], v[118:119], v[122:123]
	v_med3_f32 v134, v134, s55, v232
	v_med3_f32 v135, v135, s55, v232
	v_pk_mul_f32 v[136:137], v[170:171], s[78:79]
	v_lshl_add_u64 v[122:123], v[166:167], 1, s[30:31]
	v_exp_f32_e32 v134, v134
	v_exp_f32_e32 v135, v135
	v_med3_f32 v136, v136, s55, v232
	v_med3_f32 v137, v137, s55, v232
	v_pk_add_f32 v[126:127], v[134:135], 1.0 op_sel_hi:[1,0]
	v_pk_add_f32 v[134:135], v[134:135], 1.0 op_sel_hi:[1,0] neg_lo:[1,0] neg_hi:[1,0]
	v_exp_f32_e32 v136, v136
	v_exp_f32_e32 v137, v137
	v_pk_mul_f32 v[130:131], v[130:131], v[126:127]
	v_pk_add_f32 v[128:129], v[136:137], 1.0 op_sel_hi:[1,0]
	v_pk_add_f32 v[136:137], v[136:137], 1.0 op_sel_hi:[1,0] neg_lo:[1,0] neg_hi:[1,0]
	v_rcp_f32_e32 v130, v130
	v_rcp_f32_e32 v131, v131
	v_pk_mul_f32 v[132:133], v[132:133], v[128:129]
	v_pk_mul_f32 v[134:135], v[134:135], v[130:131]
	v_rcp_f32_e32 v132, v132
	v_rcp_f32_e32 v133, v133
	v_cvt_pk_bf16_f32 v120, v134, v135
	v_pk_mul_f32 v[136:137], v[136:137], v[132:133]
	v_pk_mul_f32 v[134:135], v[162:163], v[134:135]
	v_cvt_pk_bf16_f32 v121, v136, v137
	v_cvt_pk_bf16_f32 v116, v134, v135
	v_pk_mul_f32 v[136:137], v[164:165], v[136:137]
	global_store_dwordx2 v[122:123], v[120:121], off nt
	v_cvt_pk_bf16_f32 v117, v136, v137
	ds_write_b64 v205, v[116:117] offset:4608
	s_waitcnt lgkmcnt(0)
	s_barrier
	ds_read_b128 v[146:149], v206 offset:4608
	ds_read_b128 v[142:145], v206 offset:4672
	ds_read_b128 v[138:141], v206 offset:4736
	ds_read_b128 v[134:137], v206 offset:4800
	v_or_b32_e32 v167, 16, v233
	s_and_saveexec_b64 s[24:25], s[6:7]
	s_xor_b64 s[24:25], exec, s[24:25]
	s_cbranch_execz .LBB1_91
	s_and_saveexec_b64 s[42:43], s[8:9]
	s_xor_b64 s[42:43], exec, s[42:43]
	s_cbranch_execz .LBB1_88
	s_cmpk_eq_i32 s40, 0x1810
	s_cbranch_scc1 .LBB1_88
	s_waitcnt vmcnt(4)
	v_fma_f32 v115, v188, v178, v179
	v_max_f32_e32 v115, 0, v115
	v_mul_f32_e32 v115, 0xbfb8aa3b, v115
	v_exp_f32_e32 v115, v115
	s_bitcmp1_b32 s59, 0
	s_waitcnt vmcnt(3)
	v_fma_f32 v116, v178, v187, v179
	s_cselect_b32 s47, 0, 0x1200
	v_cvt_pk_bf16_f32 v115, v115, s0
	ds_write_b16 v213, v115
	v_max_f32_e32 v115, 0, v116
	v_cvt_pk_bf16_f32 v116, v188, s0
	v_lshl_add_u32 v117, s47, 1, v221
	v_mul_f32_e32 v115, 0xbfb8aa3b, v115
	ds_write_b16 v117, v116
	s_waitcnt vmcnt(2)
	v_fma_f32 v116, v178, v186, v179
	v_exp_f32_e32 v115, v115
	v_max_f32_e32 v116, 0, v116
	v_mul_f32_e32 v116, 0xbfb8aa3b, v116
	v_exp_f32_e32 v116, v116
	v_cvt_pk_bf16_f32 v115, v115, s0
	ds_write_b16 v213, v115 offset:3584
	v_cvt_pk_bf16_f32 v115, v187, s0
	ds_write_b16 v117, v115 offset:2304
	v_cvt_pk_bf16_f32 v115, v116, s0
	s_waitcnt vmcnt(1)
	v_fma_f32 v116, v178, v157, v179
	v_max_f32_e32 v116, 0, v116
	v_mul_f32_e32 v116, 0xbfb8aa3b, v116
	v_exp_f32_e32 v116, v116
	ds_write_b16 v213, v115 offset:7168
	v_cvt_pk_bf16_f32 v115, v186, s0
	ds_write_b16 v117, v115 offset:4608
	v_cvt_pk_bf16_f32 v115, v116, s0
	ds_write_b16 v213, v115 offset:10752
	v_cvt_pk_bf16_f32 v115, v157, s0
	ds_write_b16 v117, v115 offset:6912
	s_and_saveexec_b64 s[44:45], s[26:27]
	s_cbranch_execz .LBB1_85
	v_fma_f32 v115, v155, v180, v181
	v_max_f32_e32 v115, 0, v115
	v_mul_f32_e32 v115, 0xbfb8aa3b, v115
	v_exp_f32_e32 v115, v115
	v_fma_f32 v116, v180, v182, v181
	v_max_f32_e32 v116, 0, v116
	v_mul_f32_e32 v116, 0xbfb8aa3b, v116
	v_cvt_pk_bf16_f32 v115, v115, s0
	ds_write_b16 v214, v115
	v_exp_f32_e32 v115, v116
	v_cvt_pk_bf16_f32 v116, v155, s0
	v_lshl_add_u32 v117, s47, 1, v222
	ds_write_b16 v117, v116
	v_fma_f32 v116, v180, v183, v181
	v_max_f32_e32 v116, 0, v116
	v_mul_f32_e32 v116, 0xbfb8aa3b, v116
	v_exp_f32_e32 v116, v116
	v_cvt_pk_bf16_f32 v115, v115, s0
	ds_write_b16 v214, v115 offset:3584
	v_cvt_pk_bf16_f32 v115, v182, s0
	ds_write_b16 v117, v115 offset:2304
	v_cvt_pk_bf16_f32 v115, v116, s0
	v_fma_f32 v116, v180, v184, v181
	v_max_f32_e32 v116, 0, v116
	v_mul_f32_e32 v116, 0xbfb8aa3b, v116
	v_exp_f32_e32 v116, v116
	ds_write_b16 v214, v115 offset:7168
	v_cvt_pk_bf16_f32 v115, v183, s0
	ds_write_b16 v117, v115 offset:4608
	v_cvt_pk_bf16_f32 v115, v116, s0
	ds_write_b16 v214, v115 offset:10752
	v_cvt_pk_bf16_f32 v115, v184, s0
	ds_write_b16 v117, v115 offset:6912

.Lred_skip_1:
	s_nop 5
	v_med3_f32 v120, v120, s55, v232
	v_med3_f32 v121, v121, s55, v232
	v_mfma_f32_16x16x32_bf16 v[130:133], v[102:105], v[134:137], v[130:133]
	v_exp_f32_e32 v126, v126
	v_exp_f32_e32 v127, v127
	v_mfma_f32_16x16x32_bf16 v[130:133], v[106:109], v[138:141], v[130:133]
	v_exp_f32_e32 v116, v116
	v_exp_f32_e32 v117, v117
	v_exp_f32_e32 v120, v120
	v_exp_f32_e32 v121, v121
	v_med3_f32 v122, v122, s55, v232
	v_med3_f32 v123, v123, s55, v232
	v_pk_add_f32 v[126:127], v[126:127], 1.0 op_sel_hi:[1,0]
	v_pk_add_f32 v[134:135], v[120:121], 1.0 op_sel_hi:[1,0]
	v_pk_add_f32 v[116:117], v[116:117], 1.0 op_sel_hi:[1,0]
	v_pk_add_f32 v[120:121], v[120:121], 1.0 op_sel_hi:[1,0] neg_lo:[1,0] neg_hi:[1,0]
	v_exp_f32_e32 v128, v128
	v_exp_f32_e32 v129, v129
	v_exp_f32_e32 v118, v118
	v_exp_f32_e32 v119, v119
	v_exp_f32_e32 v122, v122
	v_exp_f32_e32 v123, v123
	v_pk_mul_f32 v[126:127], v[126:127], v[134:135]
	v_exp_f32_e32 v130, v130
	v_exp_f32_e32 v131, v131
	v_pk_add_f32 v[128:129], v[128:129], 1.0 op_sel_hi:[1,0]
	v_pk_add_f32 v[136:137], v[122:123], 1.0 op_sel_hi:[1,0]
	v_pk_add_f32 v[118:119], v[118:119], 1.0 op_sel_hi:[1,0]
	v_pk_add_f32 v[122:123], v[122:123], 1.0 op_sel_hi:[1,0] neg_lo:[1,0] neg_hi:[1,0]
	v_rcp_f32_e32 v126, v126
	v_rcp_f32_e32 v127, v127
	v_rcp_f32_e32 v116, v116
	v_rcp_f32_e32 v117, v117
	v_pk_mul_f32 v[128:129], v[128:129], v[136:137]
	v_exp_f32_e32 v132, v132
	v_exp_f32_e32 v133, v133
	v_pk_mul_f32 v[120:121], v[120:121], v[126:127]
	v_pk_add_f32 v[130:131], v[130:131], 1.0 op_sel_hi:[1,0]
	v_rcp_f32_e32 v128, v128
	v_rcp_f32_e32 v129, v129
	v_rcp_f32_e32 v118, v118
	v_rcp_f32_e32 v119, v119
	v_pk_fma_f32 v[168:169], v[168:169], v[116:117], v[120:121]
	v_pk_mul_f32 v[122:123], v[122:123], v[128:129]
	v_pk_add_f32 v[132:133], v[132:133], 1.0 op_sel_hi:[1,0]
	v_pk_mul_f32 v[134:135], v[168:169], s[78:79]
	v_pk_fma_f32 v[170:171], v[170:171], v[118:119], v[122:123]
	v_med3_f32 v134, v134, s55, v232
	v_med3_f32 v135, v135, s55, v232
	v_pk_mul_f32 v[136:137], v[170:171], s[78:79]
	v_add_u32_e32 v122, 0x80, v166
	v_mov_b32_e32 v123, v114
	v_lshl_add_u64 v[122:123], v[122:123], 1, s[30:31]
	v_exp_f32_e32 v134, v134
	v_exp_f32_e32 v135, v135
	v_med3_f32 v136, v136, s55, v232
	v_med3_f32 v137, v137, s55, v232
	v_pk_add_f32 v[126:127], v[134:135], 1.0 op_sel_hi:[1,0]
	v_pk_add_f32 v[134:135], v[134:135], 1.0 op_sel_hi:[1,0] neg_lo:[1,0] neg_hi:[1,0]
	v_exp_f32_e32 v136, v136
	v_exp_f32_e32 v137, v137
	v_pk_mul_f32 v[130:131], v[130:131], v[126:127]
	v_pk_add_f32 v[128:129], v[136:137], 1.0 op_sel_hi:[1,0]
	v_pk_add_f32 v[136:137], v[136:137], 1.0 op_sel_hi:[1,0] neg_lo:[1,0] neg_hi:[1,0]
	v_rcp_f32_e32 v130, v130
	v_rcp_f32_e32 v131, v131
	v_pk_mul_f32 v[132:133], v[132:133], v[128:129]
	v_pk_mul_f32 v[134:135], v[134:135], v[130:131]
	v_rcp_f32_e32 v132, v132
	v_rcp_f32_e32 v133, v133
	v_cvt_pk_bf16_f32 v120, v134, v135
	v_pk_mul_f32 v[136:137], v[136:137], v[132:133]
	v_pk_mul_f32 v[134:135], v[162:163], v[134:135]
	v_cvt_pk_bf16_f32 v121, v136, v137
	v_cvt_pk_bf16_f32 v116, v134, v135
	v_pk_mul_f32 v[136:137], v[164:165], v[136:137]
	global_store_dwordx2 v[122:123], v[120:121], off nt
	v_cvt_pk_bf16_f32 v117, v136, v137
	ds_write_b64 v205, v[116:117]
	s_waitcnt lgkmcnt(0)
	s_barrier
	ds_read_b128 v[146:149], v193
	ds_read_b128 v[142:145], v193 offset:64
	ds_read_b128 v[138:141], v193 offset:128
	ds_read_b128 v[134:137], v193 offset:192
	s_and_saveexec_b64 s[24:25], s[6:7]
	s_xor_b64 s[24:25], exec, s[24:25]
	s_cbranch_execz .LBB1_127
	s_and_saveexec_b64 s[42:43], s[8:9]
	s_xor_b64 s[42:43], exec, s[42:43]
	s_cbranch_execz .LBB1_124
	s_cmpk_eq_i32 s40, 0x1810
	s_cbranch_scc1 .LBB1_124
	s_bitcmp1_b32 s59, 0
	s_cselect_b32 s47, 0, 0x1c00
	s_waitcnt vmcnt(4)
	v_cvt_pk_bf16_f32 v115, v188, s0
	v_lshl_add_u32 v116, s47, 1, v223
	ds_write_b16 v116, v115 offset:80
	ds_write_b16 v213, v115 offset:80
	s_waitcnt vmcnt(3)
	v_cvt_pk_bf16_f32 v115, v187, s0
	ds_write_b16 v116, v115 offset:3664
	ds_write_b16 v215, v115 offset:80
	s_waitcnt vmcnt(2)
	v_cvt_pk_bf16_f32 v115, v186, s0
	ds_write_b16 v116, v115 offset:7248
	ds_write_b16 v216, v115 offset:80
	s_waitcnt vmcnt(1)
	v_cvt_pk_bf16_f32 v115, v157, s0
	ds_write_b16 v116, v115 offset:10832
	ds_write_b16 v217, v115 offset:80
	s_and_saveexec_b64 s[44:45], s[26:27]
	s_cbranch_execz .LBB1_121
	v_cvt_pk_bf16_f32 v115, v155, s0
	v_lshl_add_u32 v116, s47, 1, v224
	ds_write_b16 v116, v115 offset:80
	ds_write_b16 v214, v115 offset:80
	v_cvt_pk_bf16_f32 v115, v182, s0
	ds_write_b16 v116, v115 offset:3664
	ds_write_b16 v218, v115 offset:80
	v_cvt_pk_bf16_f32 v115, v183, s0
	ds_write_b16 v116, v115 offset:7248
	ds_write_b16 v219, v115 offset:80
	v_cvt_pk_bf16_f32 v115, v184, s0
	ds_write_b16 v116, v115 offset:10832
	ds_write_b16 v220, v115 offset:80

.Lred_skip_2:
	s_nop 5
	v_med3_f32 v120, v120, s55, v232
	v_med3_f32 v121, v121, s55, v232
	v_mfma_f32_16x16x32_bf16 v[130:133], v[102:105], v[134:137], v[130:133]
	v_exp_f32_e32 v126, v126
	v_exp_f32_e32 v127, v127
	v_mfma_f32_16x16x32_bf16 v[130:133], v[106:109], v[138:141], v[130:133]
	v_exp_f32_e32 v116, v116
	v_exp_f32_e32 v117, v117
	v_exp_f32_e32 v120, v120
	v_exp_f32_e32 v121, v121
	v_med3_f32 v122, v122, s55, v232
	v_med3_f32 v123, v123, s55, v232
	v_pk_add_f32 v[126:127], v[126:127], 1.0 op_sel_hi:[1,0]
	v_pk_add_f32 v[134:135], v[120:121], 1.0 op_sel_hi:[1,0]
	v_pk_add_f32 v[116:117], v[116:117], 1.0 op_sel_hi:[1,0]
	v_pk_add_f32 v[120:121], v[120:121], 1.0 op_sel_hi:[1,0] neg_lo:[1,0] neg_hi:[1,0]
	v_exp_f32_e32 v128, v128
	v_exp_f32_e32 v129, v129
	v_exp_f32_e32 v118, v118
	v_exp_f32_e32 v119, v119
	v_exp_f32_e32 v122, v122
	v_exp_f32_e32 v123, v123
	v_pk_mul_f32 v[126:127], v[126:127], v[134:135]
	v_exp_f32_e32 v130, v130
	v_exp_f32_e32 v131, v131
	v_pk_add_f32 v[128:129], v[128:129], 1.0 op_sel_hi:[1,0]
	v_pk_add_f32 v[136:137], v[122:123], 1.0 op_sel_hi:[1,0]
	v_pk_add_f32 v[118:119], v[118:119], 1.0 op_sel_hi:[1,0]
	v_pk_add_f32 v[122:123], v[122:123], 1.0 op_sel_hi:[1,0] neg_lo:[1,0] neg_hi:[1,0]
	v_rcp_f32_e32 v126, v126
	v_rcp_f32_e32 v127, v127
	v_rcp_f32_e32 v116, v116
	v_rcp_f32_e32 v117, v117
	v_pk_mul_f32 v[128:129], v[128:129], v[136:137]
	v_exp_f32_e32 v132, v132
	v_exp_f32_e32 v133, v133
	v_pk_mul_f32 v[120:121], v[120:121], v[126:127]
	v_pk_add_f32 v[130:131], v[130:131], 1.0 op_sel_hi:[1,0]
	v_rcp_f32_e32 v128, v128
	v_rcp_f32_e32 v129, v129
	v_rcp_f32_e32 v118, v118
	v_rcp_f32_e32 v119, v119
	v_pk_fma_f32 v[168:169], v[168:169], v[116:117], v[120:121]
	v_pk_mul_f32 v[122:123], v[122:123], v[128:129]
	v_pk_add_f32 v[132:133], v[132:133], 1.0 op_sel_hi:[1,0]
	v_pk_mul_f32 v[134:135], v[168:169], s[78:79]
	v_pk_fma_f32 v[170:171], v[170:171], v[118:119], v[122:123]
	v_med3_f32 v134, v134, s55, v232
	v_med3_f32 v135, v135, s55, v232
	v_pk_mul_f32 v[136:137], v[170:171], s[78:79]
	v_add_u32_e32 v122, 0x100, v166
	v_mov_b32_e32 v123, v114
	v_lshl_add_u64 v[122:123], v[122:123], 1, s[30:31]
	v_exp_f32_e32 v134, v134
	v_exp_f32_e32 v135, v135
	v_med3_f32 v136, v136, s55, v232
	v_med3_f32 v137, v137, s55, v232
	v_pk_add_f32 v[126:127], v[134:135], 1.0 op_sel_hi:[1,0]
	v_pk_add_f32 v[134:135], v[134:135], 1.0 op_sel_hi:[1,0] neg_lo:[1,0] neg_hi:[1,0]
	v_exp_f32_e32 v136, v136
	v_exp_f32_e32 v137, v137
	v_pk_mul_f32 v[130:131], v[130:131], v[126:127]
	v_pk_add_f32 v[128:129], v[136:137], 1.0 op_sel_hi:[1,0]
	v_pk_add_f32 v[136:137], v[136:137], 1.0 op_sel_hi:[1,0] neg_lo:[1,0] neg_hi:[1,0]
	v_rcp_f32_e32 v130, v130
	v_rcp_f32_e32 v131, v131
	v_pk_mul_f32 v[132:133], v[132:133], v[128:129]
	v_pk_mul_f32 v[134:135], v[134:135], v[130:131]
	v_rcp_f32_e32 v132, v132
	v_rcp_f32_e32 v133, v133
	v_cvt_pk_bf16_f32 v120, v134, v135
	v_pk_mul_f32 v[136:137], v[136:137], v[132:133]
	v_pk_mul_f32 v[134:135], v[162:163], v[134:135]
	v_cvt_pk_bf16_f32 v121, v136, v137
	v_cvt_pk_bf16_f32 v116, v134, v135
	v_pk_mul_f32 v[136:137], v[164:165], v[136:137]
	global_store_dwordx2 v[122:123], v[120:121], off nt
	v_cvt_pk_bf16_f32 v117, v136, v137
	ds_write_b64 v205, v[116:117] offset:4608
	s_waitcnt lgkmcnt(0)
	s_barrier
	ds_read_b128 v[134:137], v206 offset:4608
	ds_read_b128 v[138:141], v206 offset:4672
	ds_read_b128 v[142:145], v206 offset:4736
	ds_read_b128 v[146:149], v206 offset:4800
	s_and_saveexec_b64 s[42:43], s[6:7]
	s_xor_b64 s[42:43], exec, s[42:43]
	s_cbranch_execz .LBB1_165
	s_and_saveexec_b64 s[44:45], s[8:9]
	s_xor_b64 s[44:45], exec, s[44:45]
	s_cbranch_execz .LBB1_160
	s_andn2_b64 vcc, exec, s[24:25]
	s_cbranch_vccnz .LBB1_160
	s_andn2_b32 s49, 1, s59
	s_mulk_i32 s49, 0xd00
	v_lshl_add_u32 v115, s49, 2, v185
	v_add_u32_e32 v116, 0xec00, v115
	s_waitcnt vmcnt(3)
	ds_write2st64_b32 v115, v188, v187 offset0:236 offset1:249
	s_waitcnt vmcnt(1)
	ds_write2st64_b32 v116, v186, v157 offset0:26 offset1:39
	s_and_saveexec_b64 s[46:47], s[26:27]
	s_cbranch_execz .LBB1_194
	v_lshl_add_u32 v115, s49, 2, v225
	v_add_u32_e32 v116, 0xec00, v115
	ds_write2st64_b32 v115, v155, v182 offset0:236 offset1:249
	ds_write2st64_b32 v116, v183, v184 offset0:26 offset1:39
	s_or_b64 exec, exec, s[46:47]
	s_and_saveexec_b64 s[46:47], s[20:21]
	s_cbranch_execnz .LBB1_195

	.amdhsa_kernel _Z10rnn_kernelPKfS0_S0_S0_S0_S0_PKtS2_PfPtS3_
		.amdhsa_group_segment_fixed_size 0
		.amdhsa_private_segment_fixed_size 0
		.amdhsa_kernarg_size 88
		.amdhsa_user_sgpr_count 2
		.amdhsa_user_sgpr_dispatch_ptr 0
		.amdhsa_user_sgpr_queue_ptr 0
		.amdhsa_user_sgpr_kernarg_segment_ptr 1
		.amdhsa_user_sgpr_dispatch_id 0
		.amdhsa_user_sgpr_kernarg_preload_length 0
		.amdhsa_user_sgpr_kernarg_preload_offset 0
		.amdhsa_user_sgpr_private_segment_size 0
		.amdhsa_uses_dynamic_stack 0
		.amdhsa_enable_private_segment 0
		.amdhsa_system_sgpr_workgroup_id_x 1
		.amdhsa_system_sgpr_workgroup_id_y 0
		.amdhsa_system_sgpr_workgroup_id_z 0
		.amdhsa_system_sgpr_workgroup_info 0
		.amdhsa_system_vgpr_workitem_id 0
		.amdhsa_next_free_vgpr 250
		.amdhsa_next_free_sgpr 80
		.amdhsa_accum_offset 252
		.amdhsa_reserve_vcc 1
		.amdhsa_float_round_mode_32 0
		.amdhsa_float_round_mode_16_64 0
		.amdhsa_float_denorm_mode_32 3
		.amdhsa_float_denorm_mode_16_64 3
		.amdhsa_dx10_clamp 1
		.amdhsa_ieee_mode 1
		.amdhsa_fp16_overflow 0
		.amdhsa_tg_split 0
		.amdhsa_exception_fp_ieee_invalid_op 0
		.amdhsa_exception_fp_denorm_src 0
		.amdhsa_exception_fp_ieee_div_zero 0
		.amdhsa_exception_fp_ieee_overflow 0
		.amdhsa_exception_fp_ieee_underflow 0
		.amdhsa_exception_fp_ieee_inexact 0
		.amdhsa_exception_int_div_zero 0
	.end_amdhsa_kernel

amdhsa.kernels:
  - .agpr_count:     0
    .args:
      - .actual_access:  read_only
        .address_space:  global
        .offset:         0
        .size:           8
        .value_kind:     global_buffer
      - .actual_access:  read_only
        .address_space:  global
        .offset:         8
        .size:           8
        .value_kind:     global_buffer
      - .actual_access:  read_only
        .address_space:  global
        .offset:         16
        .size:           8
        .value_kind:     global_buffer
      - .actual_access:  read_only
        .address_space:  global
        .offset:         24
        .size:           8
        .value_kind:     global_buffer
      - .actual_access:  read_only
        .address_space:  global
        .offset:         32
        .size:           8
        .value_kind:     global_buffer
      - .actual_access:  read_only
        .address_space:  global
        .offset:         40
        .size:           8
        .value_kind:     global_buffer
      - .actual_access:  read_only
        .address_space:  global
        .offset:         48
        .size:           8
        .value_kind:     global_buffer
      - .actual_access:  read_only
        .address_space:  global
        .offset:         56
        .size:           8
        .value_kind:     global_buffer
      - .actual_access:  read_only
        .address_space:  global
        .offset:         64
        .size:           8
        .value_kind:     global_buffer
      - .actual_access:  read_only
        .address_space:  global
        .offset:         72
        .size:           8
        .value_kind:     global_buffer
      - .actual_access:  read_only
        .address_space:  global
        .offset:         80
        .size:           8
        .value_kind:     global_buffer
      - .actual_access:  read_only
        .address_space:  global
        .offset:         88
        .size:           8
        .value_kind:     global_buffer
      - .actual_access:  read_only
        .address_space:  global
        .offset:         96
        .size:           8
        .value_kind:     global_buffer
      - .actual_access:  read_only
        .address_space:  global
        .offset:         104
        .size:           8
        .value_kind:     global_buffer
      - .actual_access:  read_only
        .address_space:  global
        .offset:         112
        .size:           8
        .value_kind:     global_buffer
      - .actual_access:  read_only
        .address_space:  global
        .offset:         120
        .size:           8
        .value_kind:     global_buffer
      - .actual_access:  write_only
        .address_space:  global
        .offset:         128
        .size:           8
        .value_kind:     global_buffer
      - .actual_access:  write_only
        .address_space:  global
        .offset:         136
        .size:           8
        .value_kind:     global_buffer
      - .actual_access:  write_only
        .address_space:  global
        .offset:         144
        .size:           8
        .value_kind:     global_buffer
    .group_segment_fixed_size: 0
    .kernarg_segment_align: 8
    .kernarg_segment_size: 152
    .language:       OpenCL C
    .language_version:
      - 2
      - 0
    .max_flat_workgroup_size: 256
    .name:           _Z11prep_kernelPKfS0_S0_S0_S0_S0_S0_S0_S0_S0_S0_S0_S0_S0_S0_S0_PtS1_S1_
    .private_segment_fixed_size: 0
    .sgpr_count:     30
    .sgpr_spill_count: 0
    .symbol:         _Z11prep_kernelPKfS0_S0_S0_S0_S0_S0_S0_S0_S0_S0_S0_S0_S0_S0_S0_PtS1_S1_.kd
    .uniform_work_group_size: 1
    .uses_dynamic_stack: false
    .vgpr_count:     8
    .vgpr_spill_count: 0
    .wavefront_size: 64
  - .agpr_count:     0
    .args:
      - .actual_access:  read_only
        .address_space:  global
        .offset:         0
        .size:           8
        .value_kind:     global_buffer
      - .actual_access:  read_only
        .address_space:  global
        .offset:         8
        .size:           8
        .value_kind:     global_buffer
      - .actual_access:  read_only
        .address_space:  global
        .offset:         16
        .size:           8
        .value_kind:     global_buffer
      - .actual_access:  read_only
        .address_space:  global
        .offset:         24
        .size:           8
        .value_kind:     global_buffer
      - .actual_access:  read_only
        .address_space:  global
        .offset:         32
        .size:           8
        .value_kind:     global_buffer
      - .actual_access:  read_only
        .address_space:  global
        .offset:         40
        .size:           8
        .value_kind:     global_buffer
      - .actual_access:  read_only
        .address_space:  global
        .offset:         48
        .size:           8
        .value_kind:     global_buffer
      - .actual_access:  read_only
        .address_space:  global
        .offset:         56
        .size:           8
        .value_kind:     global_buffer
      - .actual_access:  write_only
        .address_space:  global
        .offset:         64
        .size:           8
        .value_kind:     global_buffer
      - .actual_access:  write_only
        .address_space:  global
        .offset:         72
        .size:           8
        .value_kind:     global_buffer
      - .actual_access:  write_only
        .address_space:  global
        .offset:         80
        .size:           8
        .value_kind:     global_buffer
    .group_segment_fixed_size: 0
    .kernarg_segment_align: 8
    .kernarg_segment_size: 88
    .language:       OpenCL C
    .language_version:
      - 2
      - 0
    .max_flat_workgroup_size: 512
    .name:           _Z10rnn_kernelPKfS0_S0_S0_S0_S0_PKtS2_PfPtS3_
    .private_segment_fixed_size: 0
    .sgpr_count:     86
    .sgpr_spill_count: 0
    .symbol:         _Z10rnn_kernelPKfS0_S0_S0_S0_S0_PKtS2_PfPtS3_.kd
    .uniform_work_group_size: 1
    .uses_dynamic_stack: false
    .vgpr_count:     250
    .vgpr_spill_count: 0
    .wavefront_size: 64
  - .agpr_count:     0
    .args:
      - .actual_access:  read_only
        .address_space:  global
        .offset:         0
        .size:           8
        .value_kind:     global_buffer
      - .actual_access:  read_only
        .address_space:  global
        .offset:         8
        .size:           8
        .value_kind:     global_buffer
      - .actual_access:  read_only
        .address_space:  global
        .offset:         16
        .size:           8
        .value_kind:     global_buffer
      - .actual_access:  read_only
        .address_space:  global
        .offset:         24
        .size:           8
        .value_kind:     global_buffer
      - .actual_access:  read_only
        .address_space:  global
        .offset:         32
        .size:           8
        .value_kind:     global_buffer
      - .actual_access:  write_only
        .address_space:  global
        .offset:         40
        .size:           8
        .value_kind:     global_buffer
      - .actual_access:  write_only
        .address_space:  global
        .offset:         48
        .size:           8
        .value_kind:     global_buffer
    .group_segment_fixed_size: 0
    .kernarg_segment_align: 8
    .kernarg_segment_size: 56
    .language:       OpenCL C
    .language_version:
      - 2
      - 0
    .max_flat_workgroup_size: 1024
    .name:           _Z11attn_kernelPKtS0_PKfS2_S2_PfS3_
    .private_segment_fixed_size: 0
    .sgpr_count:     30
    .sgpr_spill_count: 0
    .symbol:         _Z11attn_kernelPKtS0_PKfS2_S2_PfS3_.kd
    .uniform_work_group_size: 1
    .uses_dynamic_stack: false
    .vgpr_count:     124
    .vgpr_spill_count: 0
    .wavefront_size: 64
  - .agpr_count:     0
    .args:
      - .actual_access:  read_only
        .address_space:  global
        .offset:         0
        .size:           8
        .value_kind:     global_buffer
      - .actual_access:  read_only
        .address_space:  global
        .offset:         8
        .size:           8
        .value_kind:     global_buffer
      - .actual_access:  read_only
        .address_space:  global
        .offset:         16
        .size:           8
        .value_kind:     global_buffer
      - .actual_access:  write_only
        .address_space:  global
        .offset:         24
        .size:           8
        .value_kind:     global_buffer
    .group_segment_fixed_size: 192
    .kernarg_segment_align: 8
    .kernarg_segment_size: 32
    .language:       OpenCL C
    .language_version:
      - 2
      - 0
    .max_flat_workgroup_size: 1024
    .name:           _Z11loss_kernelPKfS0_S0_Pf
    .private_segment_fixed_size: 0
    .sgpr_count:     14
    .sgpr_spill_count: 0
    .symbol:         _Z11loss_kernelPKfS0_S0_Pf.kd
    .uniform_work_group_size: 1
    .uses_dynamic_stack: false
    .vgpr_count:     46
    .vgpr_spill_count: 0
    .wavefront_size: 64
